# w_in GEMM epilogue: the eight per-row-group sum-of-squares loads hoisted and waited once, so result stores no longer serialise on store acknowledgements
# baseline (speedup 1.0000x reference)
.LBB0_170:
	s_mov_b32 s2, s37
	s_mov_b32 s5, s33
	v_mbcnt_lo_u32_b32 v138, -1, s2
	s_lshl_b32 s2, s5, 4
	v_mbcnt_hi_u32_b32 v138, -1, v138
	s_andn2_b32 s2, s2, 63
	v_and_or_b32 v139, v138, 15, s2
	v_lshl_add_u32 v140, s22, 8, v139
	v_ashrrev_i32_e32 v141, 31, v140
	v_lshl_add_u64 v[142:143], v[140:141], 2, s[10:11]
	global_load_dword v139, v[142:143], off
	global_load_dword v151, v[142:143], off offset:64
	global_load_dword v152, v[142:143], off offset:128
	global_load_dword v153, v[142:143], off offset:192
	global_load_dword v154, v[142:143], off offset:512
	global_load_dword v155, v[142:143], off offset:576
	global_load_dword v156, v[142:143], off offset:640
	global_load_dword v157, v[142:143], off offset:704
	s_lshl_b32 s2, s4, 8
	s_lshl_b32 s4, s5, 5
	s_and_b32 s4, s4, 0x60
	v_ashrrev_i32_e32 v138, 1, v138
	s_or_b32 s2, s4, s2
	v_and_b32_e32 v138, -8, v138
	v_add_u32_e32 v138, s2, v138
	v_cmp_gt_i32_e32 vcc, s79, v138
	s_waitcnt vmcnt(0)
	v_fmamk_f32 v139, v139, 0x3a000000, v204
	v_rsq_f32_e32 v158, v139
	v_ashrrev_i32_e32 v139, 31, v138
	v_mov_b32_e32 v159, v158
	s_and_saveexec_b64 s[4:5], vcc
	s_cbranch_execz .LBB0_172
	v_mov_b32_e32 v146, v158
	v_mov_b32_e32 v147, v158
	v_pk_mul_f32 v[126:127], v[126:127], v[146:147]
	v_pk_mul_f32 v[146:147], v[122:123], v[146:147]
	v_pk_mul_f32 v[122:123], v[120:121], v[158:159]
	v_mov_b64_e32 v[120:121], s[8:9]
	v_pk_mul_f32 v[124:125], v[124:125], v[158:159]
	v_mad_i64_i32 v[120:121], s[22:23], v140, s80, v[120:121]
	v_lshl_add_u64 v[148:149], v[138:139], 1, v[120:121]
	v_cvt_pk_bf16_f32 v120, v124, v125
	v_cvt_pk_bf16_f32 v121, v126, v127
	v_cvt_pk_bf16_f32 v122, v122, v123
	v_cvt_pk_bf16_f32 v123, v146, v147
	global_store_dwordx4 v[148:149], v[120:123], off

.LBB0_174:
	s_or_b64 exec, exec, s[22:23]
	s_nop 1
	v_mov_b32_e32 v112, v151
	v_or_b32_e32 v114, 16, v140
	v_fmamk_f32 v112, v112, 0x3a000000, v204
	v_rsq_f32_e32 v112, v112
	s_nop 0
	v_mov_b32_e32 v113, v112
	s_and_saveexec_b64 s[22:23], vcc
	s_cbranch_execz .LBB0_176
	v_mov_b32_e32 v116, v112
	v_mov_b32_e32 v117, v112
	v_pk_mul_f32 v[110:111], v[110:111], v[116:117]
	v_pk_mul_f32 v[116:117], v[106:107], v[116:117]
	v_pk_mul_f32 v[106:107], v[104:105], v[112:113]
	v_mov_b64_e32 v[104:105], s[8:9]
	v_pk_mul_f32 v[108:109], v[108:109], v[112:113]
	v_mad_i64_i32 v[104:105], s[24:25], v114, s80, v[104:105]
	v_lshl_add_u64 v[118:119], v[138:139], 1, v[104:105]
	v_cvt_pk_bf16_f32 v104, v108, v109
	v_cvt_pk_bf16_f32 v105, v110, v111
	v_cvt_pk_bf16_f32 v106, v106, v107
	v_cvt_pk_bf16_f32 v107, v116, v117
	global_store_dwordx4 v[118:119], v[104:107], off

.LBB0_178:
	s_or_b64 exec, exec, s[22:23]
	s_nop 1
	v_mov_b32_e32 v96, v152
	v_or_b32_e32 v98, 32, v140
	v_fmamk_f32 v96, v96, 0x3a000000, v204
	v_rsq_f32_e32 v96, v96
	s_nop 0
	v_mov_b32_e32 v97, v96
	s_and_saveexec_b64 s[22:23], vcc
	s_cbranch_execz .LBB0_180
	v_mov_b32_e32 v100, v96
	v_mov_b32_e32 v101, v96
	v_pk_mul_f32 v[94:95], v[94:95], v[100:101]
	v_pk_mul_f32 v[100:101], v[90:91], v[100:101]
	v_pk_mul_f32 v[90:91], v[88:89], v[96:97]
	v_mov_b64_e32 v[88:89], s[8:9]
	v_pk_mul_f32 v[92:93], v[92:93], v[96:97]
	v_mad_i64_i32 v[88:89], s[24:25], v98, s80, v[88:89]
	v_lshl_add_u64 v[102:103], v[138:139], 1, v[88:89]
	v_cvt_pk_bf16_f32 v88, v92, v93
	v_cvt_pk_bf16_f32 v89, v94, v95
	v_cvt_pk_bf16_f32 v90, v90, v91
	v_cvt_pk_bf16_f32 v91, v100, v101
	global_store_dwordx4 v[102:103], v[88:91], off

.LBB0_182:
	s_or_b64 exec, exec, s[22:23]
	s_nop 1
	v_mov_b32_e32 v80, v153
	v_or_b32_e32 v82, 48, v140
	v_fmamk_f32 v80, v80, 0x3a000000, v204
	v_rsq_f32_e32 v80, v80
	s_nop 0
	v_mov_b32_e32 v81, v80
	s_and_saveexec_b64 s[22:23], vcc
	s_cbranch_execz .LBB0_184
	v_mov_b32_e32 v84, v80
	v_mov_b32_e32 v85, v80
	v_pk_mul_f32 v[78:79], v[78:79], v[84:85]
	v_pk_mul_f32 v[84:85], v[74:75], v[84:85]
	v_pk_mul_f32 v[74:75], v[72:73], v[80:81]
	v_mov_b64_e32 v[72:73], s[8:9]
	v_pk_mul_f32 v[76:77], v[76:77], v[80:81]
	v_mad_i64_i32 v[72:73], s[24:25], v82, s80, v[72:73]
	v_lshl_add_u64 v[86:87], v[138:139], 1, v[72:73]
	v_cvt_pk_bf16_f32 v72, v76, v77
	v_cvt_pk_bf16_f32 v73, v78, v79
	v_cvt_pk_bf16_f32 v74, v74, v75
	v_cvt_pk_bf16_f32 v75, v84, v85
	global_store_dwordx4 v[86:87], v[72:75], off

.LBB0_186:
	s_or_b64 exec, exec, s[22:23]
	s_nop 1
	v_mov_b32_e32 v64, v154
	v_add_u32_e32 v66, 0x80, v140
	v_fmamk_f32 v64, v64, 0x3a000000, v204
	v_rsq_f32_e32 v64, v64
	s_nop 0
	v_mov_b32_e32 v65, v64
	s_and_saveexec_b64 s[22:23], vcc
	s_cbranch_execz .LBB0_188
	v_mov_b32_e32 v68, v64
	v_mov_b32_e32 v69, v64
	v_pk_mul_f32 v[62:63], v[62:63], v[68:69]
	v_pk_mul_f32 v[68:69], v[58:59], v[68:69]
	v_pk_mul_f32 v[58:59], v[56:57], v[64:65]
	v_mov_b64_e32 v[56:57], s[8:9]
	v_pk_mul_f32 v[60:61], v[60:61], v[64:65]
	v_mad_i64_i32 v[56:57], s[24:25], v66, s80, v[56:57]
	v_lshl_add_u64 v[70:71], v[138:139], 1, v[56:57]
	v_cvt_pk_bf16_f32 v56, v60, v61
	v_cvt_pk_bf16_f32 v57, v62, v63
	v_cvt_pk_bf16_f32 v58, v58, v59
	v_cvt_pk_bf16_f32 v59, v68, v69
	global_store_dwordx4 v[70:71], v[56:59], off

.LBB0_190:
	s_or_b64 exec, exec, s[22:23]
	s_nop 1
	v_mov_b32_e32 v48, v155
	v_add_u32_e32 v50, 0x90, v140
	v_fmamk_f32 v48, v48, 0x3a000000, v204
	v_rsq_f32_e32 v48, v48
	s_nop 0
	v_mov_b32_e32 v49, v48
	s_and_saveexec_b64 s[22:23], vcc
	s_cbranch_execz .LBB0_192
	v_mov_b32_e32 v52, v48
	v_mov_b32_e32 v53, v48
	v_pk_mul_f32 v[46:47], v[46:47], v[52:53]
	v_pk_mul_f32 v[52:53], v[42:43], v[52:53]
	v_pk_mul_f32 v[42:43], v[40:41], v[48:49]
	v_mov_b64_e32 v[40:41], s[8:9]
	v_pk_mul_f32 v[44:45], v[44:45], v[48:49]
	v_mad_i64_i32 v[40:41], s[24:25], v50, s80, v[40:41]
	v_lshl_add_u64 v[54:55], v[138:139], 1, v[40:41]
	v_cvt_pk_bf16_f32 v40, v44, v45
	v_cvt_pk_bf16_f32 v41, v46, v47
	v_cvt_pk_bf16_f32 v42, v42, v43
	v_cvt_pk_bf16_f32 v43, v52, v53
	global_store_dwordx4 v[54:55], v[40:43], off

.LBB0_194:
	s_or_b64 exec, exec, s[22:23]
	s_nop 1
	v_mov_b32_e32 v32, v156
	v_add_u32_e32 v34, 0xa0, v140
	v_fmamk_f32 v32, v32, 0x3a000000, v204
	v_rsq_f32_e32 v32, v32
	s_nop 0
	v_mov_b32_e32 v33, v32
	s_and_saveexec_b64 s[22:23], vcc
	s_cbranch_execz .LBB0_196
	v_mov_b32_e32 v36, v32
	v_mov_b32_e32 v37, v32
	v_pk_mul_f32 v[30:31], v[30:31], v[36:37]
	v_pk_mul_f32 v[36:37], v[26:27], v[36:37]
	v_pk_mul_f32 v[26:27], v[24:25], v[32:33]
	v_mov_b64_e32 v[24:25], s[8:9]
	v_pk_mul_f32 v[28:29], v[28:29], v[32:33]
	v_mad_i64_i32 v[24:25], s[24:25], v34, s80, v[24:25]
	v_lshl_add_u64 v[38:39], v[138:139], 1, v[24:25]
	v_cvt_pk_bf16_f32 v24, v28, v29
	v_cvt_pk_bf16_f32 v25, v30, v31
	v_cvt_pk_bf16_f32 v26, v26, v27
	v_cvt_pk_bf16_f32 v27, v36, v37
	global_store_dwordx4 v[38:39], v[24:27], off

.LBB0_198:
	s_or_b64 exec, exec, s[22:23]
	s_nop 1
	v_mov_b32_e32 v16, v157
	v_add_u32_e32 v18, 0xb0, v140
	v_fmamk_f32 v16, v16, 0x3a000000, v204
	v_rsq_f32_e32 v16, v16
	s_nop 0
	v_mov_b32_e32 v17, v16
	s_and_saveexec_b64 s[22:23], vcc
	s_cbranch_execz .LBB0_201
	v_mov_b32_e32 v20, v16
	v_mov_b32_e32 v21, v16
	v_pk_mul_f32 v[14:15], v[14:15], v[20:21]
	v_pk_mul_f32 v[20:21], v[10:11], v[20:21]
	v_pk_mul_f32 v[10:11], v[8:9], v[16:17]
	v_mov_b64_e32 v[8:9], s[8:9]
	v_pk_mul_f32 v[12:13], v[12:13], v[16:17]
	v_mad_i64_i32 v[8:9], s[24:25], v18, s80, v[8:9]
	v_lshl_add_u64 v[22:23], v[138:139], 1, v[8:9]
	v_cvt_pk_bf16_f32 v8, v12, v13
	v_cvt_pk_bf16_f32 v9, v14, v15
	v_cvt_pk_bf16_f32 v10, v10, v11
	v_cvt_pk_bf16_f32 v11, v20, v21
	global_store_dwordx4 v[22:23], v[8:11], off
	s_or_b64 exec, exec, s[22:23]
	s_and_saveexec_b64 s[22:23], s[4:5]
	s_cbranch_execnz .LBB0_202
